# accumulator clears per GEMM unit: aligned pairs by v_mov_b64 (half the VALU instructions)
# speedup vs baseline: 1.0065x; 1.0065x over previous
; #define PG8_BAR __builtin_amdgcn_s_barrier()
;     ...
;         if (!has_next) break;
; #pragma unroll
;         for (int a = 0; a < 2; ++a)
; #pragma unroll
;             for (int b = 0; b < 2; ++b)
; #pragma unroll
;                 for (int m = 0; m < 4; ++m)
; #pragma unroll
;                     for (int n = 0; n < 2; ++n) acc[a][b][m][n] = (f32x4){0.f, 0.f, 0.f, 0.f};
;         cur = nxt; cA = nA; cB = nB; ++ui;
;         if constexpr (ALIGN_EPI) { if (wr == 1) PG8_BAR; }
.LBB0_336:
	v_mov_b32_e32 v80, 0
	v_readlane_b32 s84, v254, 2
	s_add_i32 s2, s53, 0x40080
	s_add_i32 s3, s10, 0x100
	s_mov_b32 s10, -2
	v_mov_b32_e32 v81, v80
	v_mov_b64_e32 v[82:83], 0
	v_mov_b64_e32 v[84:85], 0
	v_mov_b64_e32 v[86:87], 0
	v_mov_b64_e32 v[88:89], 0
	v_mov_b64_e32 v[90:91], 0
	v_mov_b64_e32 v[92:93], 0
	v_mov_b64_e32 v[94:95], 0
	v_mov_b64_e32 v[96:97], 0
	v_mov_b64_e32 v[98:99], 0
	v_mov_b64_e32 v[100:101], 0
	v_mov_b64_e32 v[102:103], 0
	v_mov_b64_e32 v[104:105], 0
	v_mov_b64_e32 v[106:107], 0
	v_mov_b64_e32 v[108:109], 0
	v_mov_b64_e32 v[110:111], 0
	v_mov_b64_e32 v[0:1], 0
	v_mov_b64_e32 v[2:3], 0
	v_mov_b64_e32 v[4:5], 0
	v_mov_b64_e32 v[6:7], 0
	v_mov_b64_e32 v[8:9], 0
	v_mov_b64_e32 v[10:11], 0
	v_mov_b64_e32 v[12:13], 0
	v_mov_b64_e32 v[14:15], 0
	v_mov_b64_e32 v[16:17], 0
	v_mov_b64_e32 v[18:19], 0
	v_mov_b64_e32 v[20:21], 0
	v_mov_b64_e32 v[22:23], 0
	v_mov_b64_e32 v[24:25], 0
	v_mov_b64_e32 v[26:27], 0
	v_mov_b64_e32 v[28:29], 0
	v_mov_b64_e32 v[30:31], 0
	v_mov_b64_e32 v[112:113], 0
	v_mov_b64_e32 v[114:115], 0
	v_mov_b64_e32 v[116:117], 0
	v_mov_b64_e32 v[118:119], 0
	v_mov_b64_e32 v[120:121], 0
	v_mov_b64_e32 v[122:123], 0
	v_mov_b64_e32 v[124:125], 0
	v_mov_b64_e32 v[126:127], 0
	v_mov_b64_e32 v[128:129], 0
	v_mov_b64_e32 v[130:131], 0
	v_mov_b64_e32 v[132:133], 0
	v_mov_b64_e32 v[134:135], 0
	v_mov_b64_e32 v[136:137], 0
	v_mov_b64_e32 v[138:139], 0
	v_mov_b64_e32 v[140:141], 0
	v_mov_b64_e32 v[142:143], 0
	v_mov_b64_e32 v[32:33], 0
	v_mov_b64_e32 v[34:35], 0
	v_mov_b64_e32 v[36:37], 0
	v_mov_b64_e32 v[38:39], 0
	v_mov_b64_e32 v[40:41], 0
	v_mov_b64_e32 v[42:43], 0
	v_mov_b64_e32 v[44:45], 0
	v_mov_b64_e32 v[46:47], 0
	v_mov_b64_e32 v[48:49], 0
	v_mov_b64_e32 v[50:51], 0
	v_mov_b64_e32 v[52:53], 0
	v_mov_b64_e32 v[54:55], 0
	v_mov_b64_e32 v[56:57], 0
	v_mov_b64_e32 v[58:59], 0
	v_mov_b64_e32 v[60:61], 0
	v_mov_b64_e32 v[62:63], 0
	v_readlane_b32 s86, v254, 4
	v_readlane_b32 s85, v254, 3
	v_readlane_b32 s87, v254, 5

; #define PG8_BAR __builtin_amdgcn_s_barrier()
;     ...
;         if (!has_next) break;
; #pragma unroll
;         for (int a = 0; a < 2; ++a)
; #pragma unroll
;             for (int b = 0; b < 2; ++b)
; #pragma unroll
;                 for (int m = 0; m < 4; ++m)
; #pragma unroll
;                     for (int n = 0; n < 2; ++n) acc[a][b][m][n] = (f32x4){0.f, 0.f, 0.f, 0.f};
;         cur = nxt; cA = nA; cB = nB; ++ui;
;         if constexpr (ALIGN_EPI) { if (wr == 1) PG8_BAR; }
.LBB0_958:
	v_mov_b32_e32 v0, 0
	v_readlane_b32 s72, v254, 2
	s_add_i32 s2, s70, 0x40080
	s_add_i32 s3, s69, 0x100
	s_mov_b32 s69, -2
	v_mov_b32_e32 v1, v0
	v_mov_b64_e32 v[2:3], 0
	v_mov_b64_e32 v[4:5], 0
	v_mov_b64_e32 v[6:7], 0
	v_mov_b64_e32 v[16:17], 0
	v_mov_b64_e32 v[18:19], 0
	v_mov_b64_e32 v[20:21], 0
	v_mov_b64_e32 v[22:23], 0
	v_mov_b64_e32 v[32:33], 0
	v_mov_b64_e32 v[34:35], 0
	v_mov_b64_e32 v[36:37], 0
	v_mov_b64_e32 v[38:39], 0
	v_mov_b64_e32 v[48:49], 0
	v_mov_b64_e32 v[50:51], 0
	v_mov_b64_e32 v[52:53], 0
	v_mov_b64_e32 v[54:55], 0
	v_mov_b64_e32 v[8:9], 0
	v_mov_b64_e32 v[10:11], 0
	v_mov_b64_e32 v[12:13], 0
	v_mov_b64_e32 v[14:15], 0
	v_mov_b64_e32 v[24:25], 0
	v_mov_b64_e32 v[26:27], 0
	v_mov_b64_e32 v[28:29], 0
	v_mov_b64_e32 v[30:31], 0
	v_mov_b64_e32 v[40:41], 0
	v_mov_b64_e32 v[42:43], 0
	v_mov_b64_e32 v[44:45], 0
	v_mov_b64_e32 v[46:47], 0
	v_mov_b64_e32 v[56:57], 0
	v_mov_b64_e32 v[58:59], 0
	v_mov_b64_e32 v[60:61], 0
	v_mov_b64_e32 v[62:63], 0
	v_mov_b64_e32 v[64:65], 0
	v_mov_b64_e32 v[66:67], 0
	v_mov_b64_e32 v[68:69], 0
	v_mov_b64_e32 v[70:71], 0
	v_mov_b64_e32 v[80:81], 0
	v_mov_b64_e32 v[82:83], 0
	v_mov_b64_e32 v[84:85], 0
	v_mov_b64_e32 v[86:87], 0
	v_mov_b64_e32 v[96:97], 0
	v_mov_b64_e32 v[98:99], 0
	v_mov_b64_e32 v[100:101], 0
	v_mov_b64_e32 v[102:103], 0
	v_mov_b64_e32 v[112:113], 0
	v_mov_b64_e32 v[114:115], 0
	v_mov_b64_e32 v[116:117], 0
	v_mov_b64_e32 v[118:119], 0
	v_mov_b64_e32 v[72:73], 0
	v_mov_b64_e32 v[74:75], 0
	v_mov_b64_e32 v[76:77], 0
	v_mov_b64_e32 v[78:79], 0
	v_mov_b64_e32 v[88:89], 0
	v_mov_b64_e32 v[90:91], 0
	v_mov_b64_e32 v[92:93], 0
	v_mov_b64_e32 v[94:95], 0
	v_mov_b64_e32 v[104:105], 0
	v_mov_b64_e32 v[106:107], 0
	v_mov_b64_e32 v[108:109], 0
	v_mov_b64_e32 v[110:111], 0
	v_mov_b64_e32 v[120:121], 0
	v_mov_b64_e32 v[122:123], 0
	v_mov_b64_e32 v[124:125], 0
	v_mov_b64_e32 v[126:127], 0
	v_readlane_b32 s74, v254, 4
	v_readlane_b32 s73, v254, 3
	v_readlane_b32 s75, v254, 5

; #define PG8_BAR __builtin_amdgcn_s_barrier()
;     ...
;         if (!has_next) break;
; #pragma unroll
;         for (int a = 0; a < 2; ++a)
; #pragma unroll
;             for (int b = 0; b < 2; ++b)
; #pragma unroll
;                 for (int m = 0; m < 4; ++m)
; #pragma unroll
;                     for (int n = 0; n < 2; ++n) acc[a][b][m][n] = (f32x4){0.f, 0.f, 0.f, 0.f};
;         cur = nxt; cA = nA; cB = nB; ++ui;
;         if constexpr (ALIGN_EPI) { if (wr == 1) PG8_BAR; }
.LBB0_1101:
	v_mov_b32_e32 v0, 0
	v_readlane_b32 s56, v254, 2
	s_add_i32 s2, s52, 0x80080
	s_add_i32 s3, s53, 0x100
	s_mov_b32 s52, -2
	v_mov_b32_e32 v1, v0
	v_mov_b64_e32 v[2:3], 0
	v_mov_b64_e32 v[4:5], 0
	v_mov_b64_e32 v[6:7], 0
	v_mov_b64_e32 v[8:9], 0
	v_mov_b64_e32 v[10:11], 0
	v_mov_b64_e32 v[12:13], 0
	v_mov_b64_e32 v[14:15], 0
	v_mov_b64_e32 v[16:17], 0
	v_mov_b64_e32 v[18:19], 0
	v_mov_b64_e32 v[20:21], 0
	v_mov_b64_e32 v[22:23], 0
	v_mov_b64_e32 v[24:25], 0
	v_mov_b64_e32 v[26:27], 0
	v_mov_b64_e32 v[28:29], 0
	v_mov_b64_e32 v[30:31], 0
	v_mov_b64_e32 v[32:33], 0
	v_mov_b64_e32 v[34:35], 0
	v_mov_b64_e32 v[36:37], 0
	v_mov_b64_e32 v[38:39], 0
	v_mov_b64_e32 v[40:41], 0
	v_mov_b64_e32 v[42:43], 0
	v_mov_b64_e32 v[44:45], 0
	v_mov_b64_e32 v[46:47], 0
	v_mov_b64_e32 v[48:49], 0
	v_mov_b64_e32 v[50:51], 0
	v_mov_b64_e32 v[52:53], 0
	v_mov_b64_e32 v[54:55], 0
	v_mov_b64_e32 v[56:57], 0
	v_mov_b64_e32 v[58:59], 0
	v_mov_b64_e32 v[60:61], 0
	v_mov_b64_e32 v[62:63], 0
	v_readlane_b32 s58, v254, 4
	v_readlane_b32 s57, v254, 3
	v_readlane_b32 s59, v254, 5

; #define PG8_BAR __builtin_amdgcn_s_barrier()
;     ...
;         if (!has_next) break;
; #pragma unroll
;         for (int a = 0; a < 2; ++a)
; #pragma unroll
;             for (int b = 0; b < 2; ++b)
; #pragma unroll
;                 for (int m = 0; m < 4; ++m)
; #pragma unroll
;                     for (int n = 0; n < 2; ++n) acc[a][b][m][n] = (f32x4){0.f, 0.f, 0.f, 0.f};
;         cur = nxt; cA = nA; cB = nB; ++ui;
;         if constexpr (ALIGN_EPI) { if (wr == 1) PG8_BAR; }
.LBB0_1240:
	s_lshl_b32 s2, s60, 10
	s_and_b32 s2, s2, 0x400
	s_add_i32 s66, s2, 0
	s_lshl_b32 s2, s58, 2
	s_add_i32 s67, s2, 0
	v_mov_b32_e32 v64, 0
	s_add_i32 s66, s66, 0x24800
	s_add_i32 s67, s67, 0x24040
	s_mov_b32 s68, -2
	s_mov_b32 s69, 0x70e00080
	v_mov_b32_e32 v65, v64
	v_mov_b64_e32 v[66:67], 0
	v_mov_b64_e32 v[72:73], 0
	v_mov_b64_e32 v[74:75], 0
	v_mov_b64_e32 v[80:81], 0
	v_mov_b64_e32 v[82:83], 0
	v_mov_b64_e32 v[88:89], 0
	v_mov_b64_e32 v[90:91], 0
	v_mov_b64_e32 v[96:97], 0
	v_mov_b64_e32 v[98:99], 0
	v_mov_b64_e32 v[104:105], 0
	v_mov_b64_e32 v[106:107], 0
	v_mov_b64_e32 v[112:113], 0
	v_mov_b64_e32 v[114:115], 0
	v_mov_b64_e32 v[120:121], 0
	v_mov_b64_e32 v[122:123], 0
	v_mov_b64_e32 v[68:69], 0
	v_mov_b64_e32 v[70:71], 0
	v_mov_b64_e32 v[76:77], 0
	v_mov_b64_e32 v[78:79], 0
	v_mov_b64_e32 v[84:85], 0
	v_mov_b64_e32 v[86:87], 0
	v_mov_b64_e32 v[92:93], 0
	v_mov_b64_e32 v[94:95], 0
	v_mov_b64_e32 v[100:101], 0
	v_mov_b64_e32 v[102:103], 0
	v_mov_b64_e32 v[108:109], 0
	v_mov_b64_e32 v[110:111], 0
	v_mov_b64_e32 v[116:117], 0
	v_mov_b64_e32 v[118:119], 0
	v_mov_b64_e32 v[124:125], 0
	v_mov_b64_e32 v[126:127], 0
	v_mov_b64_e32 v[128:129], 0
	v_mov_b64_e32 v[130:131], 0
	v_mov_b64_e32 v[136:137], 0
	v_mov_b64_e32 v[138:139], 0
	v_mov_b64_e32 v[144:145], 0
	v_mov_b64_e32 v[146:147], 0
	v_mov_b64_e32 v[152:153], 0
	v_mov_b64_e32 v[154:155], 0
	v_mov_b64_e32 v[160:161], 0
	v_mov_b64_e32 v[162:163], 0
	v_mov_b64_e32 v[168:169], 0
	v_mov_b64_e32 v[170:171], 0
	v_mov_b64_e32 v[176:177], 0
	v_mov_b64_e32 v[178:179], 0
	v_mov_b64_e32 v[184:185], 0
	v_mov_b64_e32 v[186:187], 0
	v_mov_b64_e32 v[132:133], 0
	v_mov_b64_e32 v[134:135], 0
	v_mov_b64_e32 v[140:141], 0
	v_mov_b64_e32 v[142:143], 0
	v_mov_b64_e32 v[148:149], 0
	v_mov_b64_e32 v[150:151], 0
	v_mov_b64_e32 v[156:157], 0
	v_mov_b64_e32 v[158:159], 0
	v_mov_b64_e32 v[164:165], 0
	v_mov_b64_e32 v[166:167], 0
	v_mov_b64_e32 v[172:173], 0
	v_mov_b64_e32 v[174:175], 0
	v_mov_b64_e32 v[180:181], 0
	v_mov_b64_e32 v[182:183], 0
	v_mov_b64_e32 v[188:189], 0
	v_mov_b64_e32 v[190:191], 0
	s_branch .LBB0_1243

; #define PG8_BAR __builtin_amdgcn_s_barrier()
;     ...
;         if (!has_next) break;
; #pragma unroll
;         for (int a = 0; a < 2; ++a)
; #pragma unroll
;             for (int b = 0; b < 2; ++b)
; #pragma unroll
;                 for (int m = 0; m < 4; ++m)
; #pragma unroll
;                     for (int n = 0; n < 2; ++n) acc[a][b][m][n] = (f32x4){0.f, 0.f, 0.f, 0.f};
;         cur = nxt; cA = nA; cB = nB; ++ui;
;         if constexpr (ALIGN_EPI) { if (wr == 1) PG8_BAR; }
.LBB0_1334:
	v_mov_b32_e32 v0, 0
	v_readlane_b32 s60, v254, 2
	s_add_i32 s3, s53, 0x40080
	s_add_i32 s53, s54, 0x100
	s_mov_b32 s54, -2
	v_mov_b32_e32 v1, v0
	v_mov_b64_e32 v[2:3], 0
	v_mov_b64_e32 v[4:5], 0
	v_mov_b64_e32 v[6:7], 0
	v_mov_b64_e32 v[16:17], 0
	v_mov_b64_e32 v[18:19], 0
	v_mov_b64_e32 v[20:21], 0
	v_mov_b64_e32 v[22:23], 0
	v_mov_b64_e32 v[32:33], 0
	v_mov_b64_e32 v[34:35], 0
	v_mov_b64_e32 v[36:37], 0
	v_mov_b64_e32 v[38:39], 0
	v_mov_b64_e32 v[48:49], 0
	v_mov_b64_e32 v[50:51], 0
	v_mov_b64_e32 v[52:53], 0
	v_mov_b64_e32 v[54:55], 0
	v_mov_b64_e32 v[8:9], 0
	v_mov_b64_e32 v[10:11], 0
	v_mov_b64_e32 v[12:13], 0
	v_mov_b64_e32 v[14:15], 0
	v_mov_b64_e32 v[24:25], 0
	v_mov_b64_e32 v[26:27], 0
	v_mov_b64_e32 v[28:29], 0
	v_mov_b64_e32 v[30:31], 0
	v_mov_b64_e32 v[40:41], 0
	v_mov_b64_e32 v[42:43], 0
	v_mov_b64_e32 v[44:45], 0
	v_mov_b64_e32 v[46:47], 0
	v_mov_b64_e32 v[56:57], 0
	v_mov_b64_e32 v[58:59], 0
	v_mov_b64_e32 v[60:61], 0
	v_mov_b64_e32 v[62:63], 0
	v_mov_b64_e32 v[64:65], 0
	v_mov_b64_e32 v[66:67], 0
	v_mov_b64_e32 v[68:69], 0
	v_mov_b64_e32 v[70:71], 0
	v_mov_b64_e32 v[80:81], 0
	v_mov_b64_e32 v[82:83], 0
	v_mov_b64_e32 v[84:85], 0
	v_mov_b64_e32 v[86:87], 0
	v_mov_b64_e32 v[96:97], 0
	v_mov_b64_e32 v[98:99], 0
	v_mov_b64_e32 v[100:101], 0
	v_mov_b64_e32 v[102:103], 0
	v_mov_b64_e32 v[112:113], 0
	v_mov_b64_e32 v[114:115], 0
	v_mov_b64_e32 v[116:117], 0
	v_mov_b64_e32 v[118:119], 0
	v_mov_b64_e32 v[72:73], 0
	v_mov_b64_e32 v[74:75], 0
	v_mov_b64_e32 v[76:77], 0
	v_mov_b64_e32 v[78:79], 0
	v_mov_b64_e32 v[88:89], 0
	v_mov_b64_e32 v[90:91], 0
	v_mov_b64_e32 v[92:93], 0
	v_mov_b64_e32 v[94:95], 0
	v_mov_b64_e32 v[104:105], 0
	v_mov_b64_e32 v[106:107], 0
	v_mov_b64_e32 v[108:109], 0
	v_mov_b64_e32 v[110:111], 0
	v_mov_b64_e32 v[120:121], 0
	v_mov_b64_e32 v[122:123], 0
	v_mov_b64_e32 v[124:125], 0
	v_mov_b64_e32 v[126:127], 0
	v_readlane_b32 s62, v254, 4
	v_readlane_b32 s61, v254, 3
	v_readlane_b32 s63, v254, 5
